# EpiGU (P7/P16) epilogue stores: per-store 64-bit address chain (v_mad_i64_i32 + 3 v_lshl_add_u64) replaced by one v_mad_u32_u24 offset with an SGPR base (saddr store)
# speedup vs baseline: 1.0030x; 1.0012x over previous
;     __device__ __forceinline__ void operator()(const f32x4 (&acc)[2][2][4][2], const Unit& u, int wr, int wc, int fr, int fq) const {
;     ...
;                 for (int m = 0; m < 4; ++m) qd[ai][m] = row_quad(ssq, u.pm * BM + ai * HALF + wr * 64 + m * 16 + fr, fq);
; #pragma unroll
;             for (int ai = 0; ai < 2; ++ai)
; #pragma unroll
;                 for (int m = 0; m < 4; ++m) asm volatile("" : "+v"(qd[ai][m]));
; #pragma unroll
;             for (int ai = 0; ai < 2; ++ai)
; #pragma unroll
;                 for (int m = 0; m < 4; ++m) xv[ai][m] = row_ms_from_quad(qd[ai][m], 1.0f / 1024.0f);
;         }
; #pragma unroll
;         for (int ai = 0; ai < 2; ++ai)
; #pragma unroll
;             for (int m = 0; m < 4; ++m) {
;                 const int row = u.pm * BM + ai * HALF + wr * 64 + m * 16 + fr;
;                 const float x = xv[ai][m], rs = __builtin_amdgcn_rsqf(x);
;                 const float ea = -1.4426950408889634f * rs;
;                 float h[8];
; #pragma unroll
;                 for (int n = 0; n < 2; ++n)
; #pragma unroll
;                     for (int j = 0; j < 4; ++j) {
;                         const float g = acc[ai][0][m][n][j], uu = acc[ai][1][m][n][j];
.LBB0_1870:
	v_lshl_add_u32 v162, s22, 8, v164
	v_or_b32_e32 v160, 16, v162
	v_or_b32_e32 v158, 32, v162
	v_or_b32_e32 v156, 48, v162
	v_add_u32_e32 v154, 0x80, v162
	v_add_u32_e32 v152, 0x90, v162
	v_add_u32_e32 v150, 0xa0, v162
	v_add_u32_e32 v148, 0xb0, v162
	v_and_b32_e32 v151, 64, v169
	v_xor_b32_e32 v149, 16, v169
	v_add_u32_e32 v151, 64, v151
	v_xor_b32_e32 v153, 32, v169
	v_cmp_lt_i32_e32 vcc, v149, v151
	v_mul_f32_e32 v120, v124, v120
	v_mul_f32_e32 v121, v125, v121
	v_cndmask_b32_e32 v149, v169, v149, vcc
	v_cmp_lt_i32_e32 vcc, v153, v151
	v_lshlrev_b32_e32 v149, 2, v149
	v_mul_f32_e32 v122, v126, v122
	v_cndmask_b32_e32 v151, v169, v153, vcc
	v_lshlrev_b32_e32 v151, 2, v151
	v_mul_f32_e32 v112, v116, v112
	v_mul_f32_e32 v113, v117, v113
	v_mul_f32_e32 v114, v118, v114
	s_lshl_b32 s22, s23, 7
	v_mul_f32_e32 v123, v127, v123
	s_ashr_i32 s23, s22, 31
	s_lshl_b64 s[22:23], s[22:23], 1
	v_mul_f32_e32 v104, v108, v104
	v_mul_f32_e32 v105, v109, v105
	v_mul_f32_e32 v106, v110, v106
	v_mul_f32_e32 v96, v100, v96
	v_mul_f32_e32 v97, v101, v97
	v_mul_f32_e32 v107, v111, v107
	v_mul_f32_e32 v98, v102, v98
	v_mul_f32_e32 v88, v92, v88
	v_mul_f32_e32 v89, v93, v89
	v_mul_f32_e32 v90, v94, v90
	v_mul_f32_e32 v80, v84, v80
	v_mul_f32_e32 v81, v85, v81
	v_mul_f32_e32 v91, v95, v91
	v_mul_f32_e32 v82, v86, v82
	v_mul_f32_e32 v72, v76, v72
	v_mul_f32_e32 v73, v77, v73
	v_mul_f32_e32 v74, v78, v74
	v_mul_f32_e32 v64, v68, v64
	v_mul_f32_e32 v65, v69, v65
	v_mul_f32_e32 v75, v79, v75
	v_mul_f32_e32 v66, v70, v66
	v_mul_f32_e32 v56, v60, v56
	v_mul_f32_e32 v57, v61, v57
	v_mul_f32_e32 v58, v62, v58
	v_mul_f32_e32 v48, v52, v48
	v_mul_f32_e32 v49, v53, v49
	v_mul_f32_e32 v59, v63, v59
	v_mul_f32_e32 v50, v54, v50
	v_mul_f32_e32 v40, v44, v40
	v_mul_f32_e32 v41, v45, v41
	v_mul_f32_e32 v42, v46, v42
	v_mul_f32_e32 v32, v36, v32
	v_mul_f32_e32 v33, v37, v33
	s_nop 0
	v_add_f32_e32 v153, v220, v221
	v_add_f32_e32 v153, v222, v153
	v_add_f32_e32 v155, v224, v225
	v_add_f32_e32 v153, v223, v153
	v_add_f32_e32 v155, v226, v155
	ds_bpermute_b32 v171, v149, v153
	v_add_f32_e32 v155, v227, v155
	ds_bpermute_b32 v172, v149, v155
	v_add_f32_e32 v157, v228, v229
	v_add_f32_e32 v157, v230, v157
	v_add_f32_e32 v159, v232, v233
	v_add_f32_e32 v159, v234, v159
	v_add_f32_e32 v157, v231, v157
	v_add_f32_e32 v159, v235, v159
	ds_bpermute_b32 v173, v149, v157
	ds_bpermute_b32 v174, v149, v159
	s_waitcnt lgkmcnt(3)
	v_add_f32_e32 v153, v153, v171
	ds_bpermute_b32 v171, v151, v153
	v_add_f32_e32 v161, v236, v237
	s_waitcnt lgkmcnt(3)
	v_add_f32_e32 v155, v155, v172
	v_add_f32_e32 v161, v238, v161
	ds_bpermute_b32 v172, v151, v155
	v_add_f32_e32 v161, v239, v161
	ds_bpermute_b32 v175, v149, v161
	s_waitcnt lgkmcnt(4)
	v_add_f32_e32 v157, v157, v173
	s_waitcnt lgkmcnt(3)
	v_add_f32_e32 v159, v159, v174
	ds_bpermute_b32 v173, v151, v157
	ds_bpermute_b32 v174, v151, v159
	v_add_f32_e32 v163, v240, v241
	s_waitcnt lgkmcnt(4)
	v_add_f32_e32 v153, v153, v171
	v_add_f32_e32 v163, v242, v163
	v_fmamk_f32 v171, v153, 0x3a800000, v170
	s_waitcnt lgkmcnt(3)
	v_add_f32_e32 v153, v155, v172
	v_add_f32_e32 v172, v244, v245
	v_add_f32_e32 v163, v243, v163
	v_add_f32_e32 v172, v246, v172
	ds_bpermute_b32 v176, v149, v163
	s_waitcnt lgkmcnt(3)
	v_add_f32_e32 v161, v161, v175
	v_add_f32_e32 v172, v247, v172
	ds_bpermute_b32 v175, v151, v161
	s_waitcnt lgkmcnt(3)
	v_add_f32_e32 v155, v157, v173
	ds_bpermute_b32 v173, v149, v172
	s_waitcnt lgkmcnt(3)
	v_add_f32_e32 v157, v159, v174
	v_add_f32_e32 v174, v248, v249
	v_add_f32_e32 v174, v250, v174
	v_add_f32_e32 v174, v251, v174
	s_waitcnt lgkmcnt(2)
	v_add_f32_e32 v163, v163, v176
	ds_bpermute_b32 v149, v149, v174
	s_waitcnt lgkmcnt(2)
	v_add_f32_e32 v159, v161, v175
	v_fmamk_f32 v161, v153, 0x3a800000, v170
	ds_bpermute_b32 v153, v151, v163
	s_waitcnt lgkmcnt(2)
	v_add_f32_e32 v172, v172, v173
	ds_bpermute_b32 v173, v151, v172
	s_waitcnt lgkmcnt(2)
	v_add_f32_e32 v149, v174, v149
	v_fmamk_f32 v155, v155, 0x3a800000, v170
	s_waitcnt lgkmcnt(1)
	v_add_f32_e32 v153, v163, v153
	ds_bpermute_b32 v163, v151, v149
	s_waitcnt lgkmcnt(1)
	v_add_f32_e32 v151, v172, v173
	v_rsq_f32_e32 v172, v171
	v_fmamk_f32 v157, v157, 0x3a800000, v170
	v_fmamk_f32 v159, v159, 0x3a800000, v170
	s_waitcnt lgkmcnt(0)
; __device__ __forceinline__ unsigned cvt_pk_bf16(float lo, float hi) { unsigned r; asm volatile("v_cvt_pk_bf16_f32 %0, %1, %2" : "=v"(r) : "v"(lo), "v"(hi)); return r; }
;     __device__ __forceinline__ void operator()(const f32x4 (&acc)[2][2][4][2], const Unit& u, int wr, int wc, int fr, int fq) const {
;     ...
;                 const float x = xv[ai][m], rs = __builtin_amdgcn_rsqf(x);
;                 const float ea = -1.4426950408889634f * rs;
;                 float h[8];
; #pragma unroll
;                 for (int n = 0; n < 2; ++n)
; #pragma unroll
;                     for (int j = 0; j < 4; ++j) {
;                         const float g = acc[ai][0][m][n][j], uu = acc[ai][1][m][n][j];
;                         const float e = __builtin_amdgcn_exp2f(g * ea);
;                         const float q = __builtin_amdgcn_rcpf(__builtin_fmaf(e, x, x));
;                         h[n * 4 + j] = (g * uu) * q;
;                     }
;                 u32x4 w; w.x = cvt_pk_bf16(h[0], h[1]); w.y = cvt_pk_bf16(h[2], h[3]); w.z = cvt_pk_bf16(h[4], h[5]); w.w = cvt_pk_bf16(h[6], h[7]);
;                 *(u32x4*)(Hd + (size_t)row * ldh + u.pn * HALF + wc * 32 + 8 * fq) = w;
	v_add_f32_e32 v149, v149, v163
	v_mul_f32_e32 v163, 0xbfb8aa3b, v172
	v_mul_f32_e32 v173, v125, v163
	v_exp_f32_e32 v173, v173
	v_mul_f32_e32 v172, v124, v163
	v_exp_f32_e32 v172, v172
	v_mul_f32_e32 v125, v127, v163
	v_fma_f32 v124, v173, v171, v171
	v_mul_f32_e32 v173, v126, v163
	v_rcp_f32_e32 v124, v124
	v_exp_f32_e32 v173, v173
	v_mul_f32_e32 v126, v117, v163
	v_exp_f32_e32 v126, v126
	v_mul_f32_e32 v121, v121, v124
	v_fma_f32 v124, v173, v171, v171
	v_rcp_f32_e32 v124, v124
	v_mul_f32_e32 v117, v118, v163
	v_exp_f32_e32 v117, v117
	v_exp_f32_e32 v125, v125
	v_mul_f32_e32 v122, v122, v124
	v_mul_f32_e32 v124, v116, v163
	v_exp_f32_e32 v124, v124
	v_fma_f32 v116, v126, v171, v171
	v_rcp_f32_e32 v116, v116
	v_fma_f32 v172, v172, v171, v171
	v_fma_f32 v124, v124, v171, v171
	v_rcp_f32_e32 v124, v124
	v_mul_f32_e32 v113, v113, v116
	v_fma_f32 v116, v117, v171, v171
	v_rcp_f32_e32 v172, v172
	v_mul_f32_e32 v112, v112, v124
	v_mul_f32_e32 v124, v119, v163
	v_exp_f32_e32 v124, v124
	v_fma_f32 v125, v125, v171, v171
	v_rcp_f32_e32 v116, v116
	v_rcp_f32_e32 v125, v125
	v_fmac_f32_e32 v171, v124, v171
	v_rcp_f32_e32 v117, v171
	v_mul_f32_e32 v120, v120, v172
	v_mul_f32_e32 v118, v114, v116
	v_mul_f32_e32 v114, v119, v115
	v_mul_f32_e32 v123, v123, v125
	v_mul_f32_e32 v117, v114, v117
	v_cvt_pk_bf16_f32 v114, v120, v121
	v_cvt_pk_bf16_f32 v115, v122, v123
	v_cvt_pk_bf16_f32 v116, v112, v113
	s_add_u32 s100, s8, s22
	s_addc_u32 s101, s9, s23
	s_add_u32 s100, s100, s4
	s_addc_u32 s101, s101, s5
	v_rsq_f32_e32 v120, v161
	v_cvt_pk_bf16_f32 v117, v118, v117
	v_mad_u32_u24 v118, v162, s47, v136
	v_mul_f32_e32 v120, 0xbfb8aa3b, v120
	global_store_dwordx4 v118, v[114:117], s[100:101]
	v_mul_f32_e32 v121, v108, v120
	v_exp_f32_e32 v121, v121
	v_mul_f32_e32 v114, v109, v120
	v_exp_f32_e32 v114, v114
	v_mul_f32_e32 v109, v111, v120
	v_exp_f32_e32 v109, v109
	v_fma_f32 v115, v121, v161, v161
	v_fma_f32 v108, v114, v161, v161
	v_mul_f32_e32 v114, v110, v120
	v_rcp_f32_e32 v108, v108
	v_exp_f32_e32 v114, v114
	v_mul_f32_e32 v110, v101, v120
	v_exp_f32_e32 v110, v110
	v_mul_f32_e32 v105, v105, v108
	v_fma_f32 v108, v114, v161, v161
	v_rcp_f32_e32 v108, v108
	v_fma_f32 v109, v109, v161, v161
	v_mul_f32_e32 v101, v102, v120
	v_rcp_f32_e32 v109, v109
	v_mul_f32_e32 v106, v106, v108
	v_mul_f32_e32 v108, v100, v120
	v_exp_f32_e32 v108, v108
	v_exp_f32_e32 v101, v101
	v_mul_f32_e32 v107, v107, v109
	v_rcp_f32_e32 v115, v115
	v_fma_f32 v108, v108, v161, v161
	v_rcp_f32_e32 v108, v108
	v_rsq_f32_e32 v102, v155
	v_mul_f32_e32 v104, v104, v115
	v_fmamk_f32 v153, v153, 0x3a800000, v170
	v_mul_f32_e32 v100, v96, v108
	v_fma_f32 v96, v110, v161, v161
	v_rcp_f32_e32 v96, v96
	v_mul_f32_e32 v108, v103, v120
	v_exp_f32_e32 v108, v108
	v_mul_f32_e32 v102, 0xbfb8aa3b, v102
	v_mul_f32_e32 v109, v97, v96
	v_fma_f32 v96, v101, v161, v161
	v_rcp_f32_e32 v96, v96
	v_fmac_f32_e32 v161, v108, v161
	v_rcp_f32_e32 v97, v161
	v_mul_f32_e32 v43, v47, v43
	v_mul_f32_e32 v101, v98, v96
	v_mul_f32_e32 v96, v103, v99
	v_mul_f32_e32 v99, v96, v97
	v_cvt_pk_bf16_f32 v96, v104, v105
	v_cvt_pk_bf16_f32 v97, v106, v107
	v_cvt_pk_bf16_f32 v98, v100, v109
	v_cvt_pk_bf16_f32 v99, v101, v99
	v_mad_u32_u24 v100, v160, s47, v136
	global_store_dwordx4 v100, v[96:99], s[100:101]
	v_mul_f32_e32 v103, v92, v102
	v_exp_f32_e32 v103, v103
	v_mul_f32_e32 v96, v93, v102
	v_exp_f32_e32 v96, v96
	v_mul_f32_e32 v93, v95, v102
	v_exp_f32_e32 v93, v93
	v_fma_f32 v97, v103, v155, v155
	v_fma_f32 v92, v96, v155, v155
	v_mul_f32_e32 v96, v94, v102
	v_rcp_f32_e32 v92, v92
	v_exp_f32_e32 v96, v96
	v_mul_f32_e32 v94, v85, v102
	v_exp_f32_e32 v94, v94
	v_mul_f32_e32 v89, v89, v92
	v_fma_f32 v92, v96, v155, v155
	v_rcp_f32_e32 v92, v92
	v_fma_f32 v93, v93, v155, v155
	v_mul_f32_e32 v85, v86, v102
	v_rcp_f32_e32 v93, v93
	v_mul_f32_e32 v90, v90, v92
	v_mul_f32_e32 v92, v84, v102
	v_exp_f32_e32 v92, v92
	v_exp_f32_e32 v85, v85
	v_mul_f32_e32 v91, v91, v93
	v_rcp_f32_e32 v97, v97
	v_fma_f32 v92, v92, v155, v155
	v_rcp_f32_e32 v92, v92
	v_rsq_f32_e32 v86, v157
	v_mul_f32_e32 v88, v88, v97
	v_mul_f32_e32 v34, v38, v34
	v_mul_f32_e32 v84, v80, v92
	v_fma_f32 v80, v94, v155, v155
	v_rcp_f32_e32 v80, v80
	v_mul_f32_e32 v92, v87, v102
	v_exp_f32_e32 v92, v92
	v_mul_f32_e32 v86, 0xbfb8aa3b, v86
	v_mul_f32_e32 v93, v81, v80
	v_fma_f32 v80, v85, v155, v155
	v_rcp_f32_e32 v80, v80
	v_fmac_f32_e32 v155, v92, v155
	v_rcp_f32_e32 v81, v155
	v_fmamk_f32 v151, v151, 0x3a800000, v170
	v_mul_f32_e32 v85, v82, v80
	v_mul_f32_e32 v80, v87, v83
	v_mul_f32_e32 v83, v80, v81
	v_cvt_pk_bf16_f32 v80, v88, v89
	v_cvt_pk_bf16_f32 v81, v90, v91
	v_cvt_pk_bf16_f32 v82, v84, v93
	v_cvt_pk_bf16_f32 v83, v85, v83
	v_mad_u32_u24 v84, v158, s47, v136
	global_store_dwordx4 v84, v[80:83], s[100:101]
	v_mul_f32_e32 v87, v76, v86
	v_exp_f32_e32 v87, v87
	v_mul_f32_e32 v80, v77, v86
	v_exp_f32_e32 v80, v80
	v_mul_f32_e32 v77, v79, v86
	v_exp_f32_e32 v77, v77
	v_fma_f32 v81, v87, v157, v157
	v_fma_f32 v76, v80, v157, v157
	v_mul_f32_e32 v80, v78, v86
	v_rcp_f32_e32 v76, v76
	v_exp_f32_e32 v80, v80
	v_mul_f32_e32 v78, v69, v86
	v_exp_f32_e32 v78, v78
	v_mul_f32_e32 v73, v73, v76
	v_fma_f32 v76, v80, v157, v157
	v_rcp_f32_e32 v76, v76
	v_fma_f32 v77, v77, v157, v157
	v_mul_f32_e32 v69, v70, v86
	v_rcp_f32_e32 v77, v77
	v_mul_f32_e32 v74, v74, v76
	v_mul_f32_e32 v76, v68, v86
	v_exp_f32_e32 v76, v76
	v_exp_f32_e32 v69, v69
	v_mul_f32_e32 v75, v75, v77
	v_rcp_f32_e32 v81, v81
	v_fma_f32 v76, v76, v157, v157
	v_rcp_f32_e32 v76, v76
	v_rsq_f32_e32 v70, v159
	v_mul_f32_e32 v72, v72, v81
	v_mul_f32_e32 v24, v28, v24
	v_mul_f32_e32 v68, v64, v76
	v_fma_f32 v64, v78, v157, v157
; __device__ __forceinline__ unsigned cvt_pk_bf16(float lo, float hi) { unsigned r; asm volatile("v_cvt_pk_bf16_f32 %0, %1, %2" : "=v"(r) : "v"(lo), "v"(hi)); return r; }
;     __device__ __forceinline__ void operator()(const f32x4 (&acc)[2][2][4][2], const Unit& u, int wr, int wc, int fr, int fq) const {
;     ...
;             for (int m = 0; m < 4; ++m) {
;                 const int row = u.pm * BM + ai * HALF + wr * 64 + m * 16 + fr;
;                 const float x = xv[ai][m], rs = __builtin_amdgcn_rsqf(x);
;                 const float ea = -1.4426950408889634f * rs;
;                 float h[8];
; #pragma unroll
;                 for (int n = 0; n < 2; ++n)
; #pragma unroll
;                     for (int j = 0; j < 4; ++j) {
;                         const float g = acc[ai][0][m][n][j], uu = acc[ai][1][m][n][j];
;                         const float e = __builtin_amdgcn_exp2f(g * ea);
;                         const float q = __builtin_amdgcn_rcpf(__builtin_fmaf(e, x, x));
;                         h[n * 4 + j] = (g * uu) * q;
;                     }
;                 u32x4 w; w.x = cvt_pk_bf16(h[0], h[1]); w.y = cvt_pk_bf16(h[2], h[3]); w.z = cvt_pk_bf16(h[4], h[5]); w.w = cvt_pk_bf16(h[6], h[7]);
;                 *(u32x4*)(Hd + (size_t)row * ldh + u.pn * HALF + wc * 32 + 8 * fq) = w;
;             }
	v_rcp_f32_e32 v64, v64
	v_mul_f32_e32 v76, v71, v86
	v_exp_f32_e32 v76, v76
	v_mul_f32_e32 v70, 0xbfb8aa3b, v70
	v_mul_f32_e32 v77, v65, v64
	v_fma_f32 v64, v69, v157, v157
	v_rcp_f32_e32 v64, v64
	v_fmac_f32_e32 v157, v76, v157
	v_rcp_f32_e32 v65, v157
	v_mul_f32_e32 v25, v29, v25
	v_mul_f32_e32 v69, v66, v64
	v_mul_f32_e32 v64, v71, v67
	v_mul_f32_e32 v67, v64, v65
	v_cvt_pk_bf16_f32 v64, v72, v73
	v_cvt_pk_bf16_f32 v65, v74, v75
	v_cvt_pk_bf16_f32 v66, v68, v77
	v_cvt_pk_bf16_f32 v67, v69, v67
	v_mad_u32_u24 v68, v156, s47, v136
	global_store_dwordx4 v68, v[64:67], s[100:101]
	v_mul_f32_e32 v71, v60, v70
	v_exp_f32_e32 v71, v71
	v_mul_f32_e32 v64, v61, v70
	v_exp_f32_e32 v64, v64
	v_mul_f32_e32 v61, v63, v70
	v_exp_f32_e32 v61, v61
	v_fma_f32 v65, v71, v159, v159
	v_fma_f32 v60, v64, v159, v159
	v_mul_f32_e32 v64, v62, v70
	v_rcp_f32_e32 v60, v60
	v_exp_f32_e32 v64, v64
	v_mul_f32_e32 v62, v53, v70
	v_exp_f32_e32 v62, v62
	v_mul_f32_e32 v57, v57, v60
	v_fma_f32 v60, v64, v159, v159
	v_rcp_f32_e32 v60, v60
	v_fma_f32 v61, v61, v159, v159
	v_mul_f32_e32 v53, v54, v70
	v_rcp_f32_e32 v61, v61
	v_mul_f32_e32 v58, v58, v60
	v_mul_f32_e32 v60, v52, v70
	v_exp_f32_e32 v60, v60
	v_exp_f32_e32 v53, v53
	v_mul_f32_e32 v59, v59, v61
	v_rcp_f32_e32 v65, v65
	v_fma_f32 v60, v60, v159, v159
	v_rcp_f32_e32 v60, v60
	v_rsq_f32_e32 v54, v153
	v_mul_f32_e32 v56, v56, v65
	v_mul_f32_e32 v26, v30, v26
	v_mul_f32_e32 v52, v48, v60
	v_fma_f32 v48, v62, v159, v159
	v_rcp_f32_e32 v48, v48
	v_mul_f32_e32 v60, v55, v70
	v_exp_f32_e32 v60, v60
	v_mul_f32_e32 v54, 0xbfb8aa3b, v54
	v_mul_f32_e32 v61, v49, v48
	v_fma_f32 v48, v53, v159, v159
	v_rcp_f32_e32 v48, v48
	v_fmac_f32_e32 v159, v60, v159
	v_rcp_f32_e32 v49, v159
	v_mul_f32_e32 v16, v20, v16
	v_mul_f32_e32 v53, v50, v48
	v_mul_f32_e32 v48, v55, v51
	v_mul_f32_e32 v51, v48, v49
	v_cvt_pk_bf16_f32 v48, v56, v57
	v_cvt_pk_bf16_f32 v49, v58, v59
	v_cvt_pk_bf16_f32 v50, v52, v61
	v_cvt_pk_bf16_f32 v51, v53, v51
	v_mad_u32_u24 v52, v154, s47, v136
	global_store_dwordx4 v52, v[48:51], s[100:101]
	v_mul_f32_e32 v55, v44, v54
	v_exp_f32_e32 v55, v55
	v_mul_f32_e32 v48, v45, v54
	v_exp_f32_e32 v48, v48
	v_mul_f32_e32 v45, v47, v54
	v_exp_f32_e32 v45, v45
	v_fma_f32 v49, v55, v153, v153
	v_fma_f32 v44, v48, v153, v153
	v_mul_f32_e32 v48, v46, v54
	v_rcp_f32_e32 v44, v44
	v_exp_f32_e32 v48, v48
	v_mul_f32_e32 v46, v37, v54
	v_exp_f32_e32 v46, v46
	v_mul_f32_e32 v41, v41, v44
	v_fma_f32 v44, v48, v153, v153
	v_rcp_f32_e32 v44, v44
	v_fma_f32 v45, v45, v153, v153
	v_mul_f32_e32 v37, v38, v54
	v_rcp_f32_e32 v45, v45
	v_mul_f32_e32 v42, v42, v44
	v_mul_f32_e32 v44, v36, v54
	v_exp_f32_e32 v44, v44
	v_exp_f32_e32 v37, v37
	v_mul_f32_e32 v43, v43, v45
	v_rcp_f32_e32 v49, v49
	v_fma_f32 v44, v44, v153, v153
	v_rcp_f32_e32 v44, v44
	v_rsq_f32_e32 v38, v151
	v_mul_f32_e32 v40, v40, v49
	v_mul_f32_e32 v17, v21, v17
	v_mul_f32_e32 v36, v32, v44
	v_fma_f32 v32, v46, v153, v153
	v_rcp_f32_e32 v32, v32
	v_mul_f32_e32 v44, v39, v54
	v_exp_f32_e32 v44, v44
	v_mul_f32_e32 v38, 0xbfb8aa3b, v38
	v_mul_f32_e32 v45, v33, v32
	v_fma_f32 v32, v37, v153, v153
	v_rcp_f32_e32 v32, v32
	v_fmac_f32_e32 v153, v44, v153
	v_rcp_f32_e32 v33, v153
	v_mul_f32_e32 v27, v31, v27
	v_mul_f32_e32 v37, v34, v32
	v_mul_f32_e32 v32, v39, v35
	v_mul_f32_e32 v35, v32, v33
	v_cvt_pk_bf16_f32 v32, v40, v41
	v_cvt_pk_bf16_f32 v33, v42, v43
	v_cvt_pk_bf16_f32 v34, v36, v45
	v_cvt_pk_bf16_f32 v35, v37, v35
	v_mad_u32_u24 v36, v152, s47, v136
	global_store_dwordx4 v36, v[32:35], s[100:101]
	v_mul_f32_e32 v39, v28, v38
	v_exp_f32_e32 v39, v39
	v_mul_f32_e32 v32, v29, v38
	v_exp_f32_e32 v32, v32
	v_mul_f32_e32 v29, v31, v38
	v_exp_f32_e32 v29, v29
	v_fma_f32 v33, v39, v151, v151
	v_fma_f32 v28, v32, v151, v151
	v_mul_f32_e32 v32, v30, v38
	v_rcp_f32_e32 v28, v28
	v_exp_f32_e32 v32, v32
	v_mul_f32_e32 v30, v21, v38
	v_exp_f32_e32 v30, v30
	v_mul_f32_e32 v25, v25, v28
	v_fma_f32 v28, v32, v151, v151
	v_rcp_f32_e32 v28, v28
	v_fma_f32 v29, v29, v151, v151
	v_mul_f32_e32 v21, v22, v38
	v_rcp_f32_e32 v29, v29
	v_mul_f32_e32 v26, v26, v28
	v_mul_f32_e32 v28, v20, v38
	v_exp_f32_e32 v28, v28
	v_exp_f32_e32 v21, v21
	v_mul_f32_e32 v27, v27, v29
	v_rcp_f32_e32 v33, v33
	v_fma_f32 v28, v28, v151, v151
	v_rcp_f32_e32 v28, v28
	v_mul_f32_e32 v18, v22, v18
	v_fmamk_f32 v149, v149, 0x3a800000, v170
	v_rsq_f32_e32 v22, v149
	v_mul_f32_e32 v20, v16, v28
	v_fma_f32 v16, v30, v151, v151
	v_rcp_f32_e32 v16, v16
	v_mul_f32_e32 v28, v23, v38
	v_exp_f32_e32 v28, v28
	v_mul_f32_e32 v24, v24, v33
	v_mul_f32_e32 v29, v17, v16
	v_fma_f32 v16, v21, v151, v151
	v_rcp_f32_e32 v16, v16
	v_fmac_f32_e32 v151, v28, v151
	v_rcp_f32_e32 v17, v151
	v_mul_f32_e32 v22, 0xbfb8aa3b, v22
	v_mul_f32_e32 v21, v18, v16
	v_mul_f32_e32 v16, v23, v19
	v_mul_f32_e32 v19, v16, v17
	v_cvt_pk_bf16_f32 v16, v24, v25
	v_cvt_pk_bf16_f32 v17, v26, v27
	v_cvt_pk_bf16_f32 v18, v20, v29
	v_cvt_pk_bf16_f32 v19, v21, v19
	v_mad_u32_u24 v20, v150, s47, v136
	global_store_dwordx4 v20, v[16:19], s[100:101]
	v_mul_f32_e32 v23, v12, v22
	v_mul_f32_e32 v8, v12, v8
	v_mul_f32_e32 v16, v13, v22
	v_exp_f32_e32 v16, v16
	v_mul_f32_e32 v9, v13, v9
	v_mul_f32_e32 v10, v14, v10
	v_mul_f32_e32 v13, v15, v22
	v_fma_f32 v12, v16, v149, v149
	v_mul_f32_e32 v16, v14, v22
	v_rcp_f32_e32 v12, v12
	v_exp_f32_e32 v16, v16
	v_mul_f32_e32 v14, v5, v22
	v_exp_f32_e32 v13, v13
	v_mul_f32_e32 v9, v9, v12
	v_fma_f32 v12, v16, v149, v149
	v_rcp_f32_e32 v12, v12
	v_exp_f32_e32 v14, v14
	v_mul_f32_e32 v0, v4, v0
	v_fma_f32 v13, v13, v149, v149
	v_mul_f32_e32 v10, v10, v12
	v_mul_f32_e32 v12, v4, v22
	v_exp_f32_e32 v12, v12
	v_mul_f32_e32 v1, v5, v1
	v_mul_f32_e32 v5, v6, v22
	v_rcp_f32_e32 v13, v13
	v_fma_f32 v12, v12, v149, v149
	v_rcp_f32_e32 v12, v12
	v_exp_f32_e32 v5, v5
	v_exp_f32_e32 v23, v23
	v_mul_f32_e32 v11, v15, v11
	v_mul_f32_e32 v4, v0, v12
	v_fma_f32 v0, v14, v149, v149
	v_rcp_f32_e32 v0, v0
	v_mul_f32_e32 v12, v7, v22
	v_exp_f32_e32 v12, v12
	v_mul_f32_e32 v11, v11, v13
	v_mul_f32_e32 v13, v1, v0
	v_fma_f32 v0, v5, v149, v149
	v_fma_f32 v17, v23, v149, v149
	v_rcp_f32_e32 v0, v0
	v_fmac_f32_e32 v149, v12, v149
	v_rcp_f32_e32 v1, v149
	v_rcp_f32_e32 v17, v17
	v_mul_f32_e32 v2, v6, v2
	v_mul_f32_e32 v5, v2, v0
	v_mul_f32_e32 v0, v7, v3
	v_mul_f32_e32 v3, v0, v1
	v_mul_f32_e32 v8, v8, v17
	v_cvt_pk_bf16_f32 v0, v8, v9
	v_cvt_pk_bf16_f32 v1, v10, v11
	v_cvt_pk_bf16_f32 v2, v4, v13
	v_cvt_pk_bf16_f32 v3, v5, v3
	v_mad_u32_u24 v4, v148, s47, v136
	s_andn2_b64 vcc, exec, s[2:3]
	s_mov_b64 s[2:3], -1
	global_store_dwordx4 v4, v[0:3], s[100:101]
	s_cbranch_vccnz .LBB0_1863
	s_andn2_b64 vcc, exec, s[6:7]
	s_cbranch_vccnz .LBB0_1862
	s_barrier
	s_branch .LBB0_1862

;     __device__ __forceinline__ void operator()(const f32x4 (&acc)[2][2][4][2], const Unit& u, int wr, int wc, int fr, int fq) const {
;     ...
;         {
;             f32x4 qd[2][4];
; #pragma unroll
;             for (int ai = 0; ai < 2; ++ai)
; #pragma unroll
;                 for (int m = 0; m < 4; ++m) qd[ai][m] = row_quad(ssq, u.pm * BM + ai * HALF + wr * 64 + m * 16 + fr, fq);
; #pragma unroll
;             for (int ai = 0; ai < 2; ++ai)
; #pragma unroll
;                 for (int m = 0; m < 4; ++m) asm volatile("" : "+v"(qd[ai][m]));
; #pragma unroll
;             for (int ai = 0; ai < 2; ++ai)
; #pragma unroll
;                 for (int m = 0; m < 4; ++m) xv[ai][m] = row_ms_from_quad(qd[ai][m], 1.0f / 1024.0f);
;         }
; #pragma unroll
;         for (int ai = 0; ai < 2; ++ai)
; #pragma unroll
;             for (int m = 0; m < 4; ++m) {
;                 const int row = u.pm * BM + ai * HALF + wr * 64 + m * 16 + fr;
;                 const float x = xv[ai][m], rs = __builtin_amdgcn_rsqf(x);
;     ...
;                         const float g = acc[ai][0][m][n][j], uu = acc[ai][1][m][n][j];
;                         const float e = __builtin_amdgcn_exp2f(g * ea);
;                         const float q = __builtin_amdgcn_rcpf(__builtin_fmaf(e, x, x));
;                         h[n * 4 + j] = (g * uu) * q;
.LBB0_2815:
	v_lshl_add_u32 v162, s22, 8, v164
	v_or_b32_e32 v160, 16, v162
	v_or_b32_e32 v158, 32, v162
	v_or_b32_e32 v156, 48, v162
	v_add_u32_e32 v154, 0x80, v162
	v_add_u32_e32 v152, 0x90, v162
	v_add_u32_e32 v150, 0xa0, v162
	v_add_u32_e32 v148, 0xb0, v162
	v_and_b32_e32 v151, 64, v169
	v_xor_b32_e32 v149, 16, v169
	v_add_u32_e32 v151, 64, v151
	v_xor_b32_e32 v153, 32, v169
	v_cmp_lt_i32_e32 vcc, v149, v151
	v_mul_f32_e32 v120, v124, v120
	v_mul_f32_e32 v121, v125, v121
	v_cndmask_b32_e32 v149, v169, v149, vcc
	v_cmp_lt_i32_e32 vcc, v153, v151
	v_lshlrev_b32_e32 v149, 2, v149
	v_mul_f32_e32 v122, v126, v122
	v_cndmask_b32_e32 v151, v169, v153, vcc
	v_lshlrev_b32_e32 v151, 2, v151
	v_mul_f32_e32 v112, v116, v112
	v_mul_f32_e32 v113, v117, v113
	v_mul_f32_e32 v114, v118, v114
	s_lshl_b32 s22, s23, 7
	v_mul_f32_e32 v123, v127, v123
	s_ashr_i32 s23, s22, 31
	s_lshl_b64 s[22:23], s[22:23], 1
	v_mul_f32_e32 v104, v108, v104
	v_mul_f32_e32 v105, v109, v105
	v_mul_f32_e32 v106, v110, v106
	v_mul_f32_e32 v96, v100, v96
	v_mul_f32_e32 v97, v101, v97
	v_mul_f32_e32 v107, v111, v107
	v_mul_f32_e32 v98, v102, v98
	v_mul_f32_e32 v88, v92, v88
	v_mul_f32_e32 v89, v93, v89
	v_mul_f32_e32 v90, v94, v90
	v_mul_f32_e32 v80, v84, v80
	v_mul_f32_e32 v81, v85, v81
	v_mul_f32_e32 v91, v95, v91
	v_mul_f32_e32 v82, v86, v82
	v_mul_f32_e32 v72, v76, v72
	v_mul_f32_e32 v73, v77, v73
	v_mul_f32_e32 v74, v78, v74
	v_mul_f32_e32 v64, v68, v64
	v_mul_f32_e32 v65, v69, v65
	v_mul_f32_e32 v75, v79, v75
	v_mul_f32_e32 v66, v70, v66
	v_mul_f32_e32 v56, v60, v56
	v_mul_f32_e32 v57, v61, v57
	v_mul_f32_e32 v58, v62, v58
	v_mul_f32_e32 v48, v52, v48
	v_mul_f32_e32 v49, v53, v49
	v_mul_f32_e32 v59, v63, v59
	v_mul_f32_e32 v50, v54, v50
	v_mul_f32_e32 v40, v44, v40
	v_mul_f32_e32 v41, v45, v41
	v_mul_f32_e32 v42, v46, v42
	v_mul_f32_e32 v32, v36, v32
	v_mul_f32_e32 v33, v37, v33
	s_nop 0
	v_add_f32_e32 v153, v220, v221
	v_add_f32_e32 v153, v222, v153
	v_add_f32_e32 v155, v224, v225
	v_add_f32_e32 v153, v223, v153
	v_add_f32_e32 v155, v226, v155
	ds_bpermute_b32 v171, v149, v153
	v_add_f32_e32 v155, v227, v155
	ds_bpermute_b32 v172, v149, v155
	v_add_f32_e32 v157, v228, v229
	v_add_f32_e32 v157, v230, v157
	v_add_f32_e32 v159, v232, v233
	v_add_f32_e32 v159, v234, v159
	v_add_f32_e32 v157, v231, v157
	v_add_f32_e32 v159, v235, v159
	ds_bpermute_b32 v173, v149, v157
	ds_bpermute_b32 v174, v149, v159
	s_waitcnt lgkmcnt(3)
	v_add_f32_e32 v153, v153, v171
	ds_bpermute_b32 v171, v151, v153
	v_add_f32_e32 v161, v236, v237
	s_waitcnt lgkmcnt(3)
	v_add_f32_e32 v155, v155, v172
	v_add_f32_e32 v161, v238, v161
	ds_bpermute_b32 v172, v151, v155
	v_add_f32_e32 v161, v239, v161
	ds_bpermute_b32 v175, v149, v161
	s_waitcnt lgkmcnt(4)
	v_add_f32_e32 v157, v157, v173
	s_waitcnt lgkmcnt(3)
	v_add_f32_e32 v159, v159, v174
	ds_bpermute_b32 v173, v151, v157
	ds_bpermute_b32 v174, v151, v159
	v_add_f32_e32 v163, v240, v241
	s_waitcnt lgkmcnt(4)
	v_add_f32_e32 v153, v153, v171
	v_add_f32_e32 v163, v242, v163
	v_fmamk_f32 v171, v153, 0x3a800000, v170
	s_waitcnt lgkmcnt(3)
	v_add_f32_e32 v153, v155, v172
	v_add_f32_e32 v172, v244, v245
	v_add_f32_e32 v163, v243, v163
	v_add_f32_e32 v172, v246, v172
	ds_bpermute_b32 v176, v149, v163
	s_waitcnt lgkmcnt(3)
	v_add_f32_e32 v161, v161, v175
	v_add_f32_e32 v172, v247, v172
	ds_bpermute_b32 v175, v151, v161
	s_waitcnt lgkmcnt(3)
	v_add_f32_e32 v155, v157, v173
	ds_bpermute_b32 v173, v149, v172
	s_waitcnt lgkmcnt(3)
	v_add_f32_e32 v157, v159, v174
	v_add_f32_e32 v174, v248, v249
	v_add_f32_e32 v174, v250, v174
	v_add_f32_e32 v174, v251, v174
	s_waitcnt lgkmcnt(2)
	v_add_f32_e32 v163, v163, v176
	ds_bpermute_b32 v149, v149, v174
	s_waitcnt lgkmcnt(2)
	v_add_f32_e32 v159, v161, v175
	v_fmamk_f32 v161, v153, 0x3a800000, v170
	ds_bpermute_b32 v153, v151, v163
	s_waitcnt lgkmcnt(2)
	v_add_f32_e32 v172, v172, v173
	ds_bpermute_b32 v173, v151, v172
	s_waitcnt lgkmcnt(2)
	v_add_f32_e32 v149, v174, v149
	v_fmamk_f32 v155, v155, 0x3a800000, v170
	s_waitcnt lgkmcnt(1)
	v_add_f32_e32 v153, v163, v153
	ds_bpermute_b32 v163, v151, v149
	s_waitcnt lgkmcnt(1)
	v_add_f32_e32 v151, v172, v173
	v_rsq_f32_e32 v172, v171
	v_fmamk_f32 v157, v157, 0x3a800000, v170
	v_fmamk_f32 v159, v159, 0x3a800000, v170
	s_waitcnt lgkmcnt(0)
; __device__ __forceinline__ unsigned cvt_pk_bf16(float lo, float hi) { unsigned r; asm volatile("v_cvt_pk_bf16_f32 %0, %1, %2" : "=v"(r) : "v"(lo), "v"(hi)); return r; }
;     __device__ __forceinline__ void operator()(const f32x4 (&acc)[2][2][4][2], const Unit& u, int wr, int wc, int fr, int fq) const {
;     ...
;             for (int m = 0; m < 4; ++m) {
;                 const int row = u.pm * BM + ai * HALF + wr * 64 + m * 16 + fr;
;                 const float x = xv[ai][m], rs = __builtin_amdgcn_rsqf(x);
;                 const float ea = -1.4426950408889634f * rs;
;                 float h[8];
; #pragma unroll
;                 for (int n = 0; n < 2; ++n)
; #pragma unroll
;                     for (int j = 0; j < 4; ++j) {
;                         const float g = acc[ai][0][m][n][j], uu = acc[ai][1][m][n][j];
;                         const float e = __builtin_amdgcn_exp2f(g * ea);
;                         const float q = __builtin_amdgcn_rcpf(__builtin_fmaf(e, x, x));
;                         h[n * 4 + j] = (g * uu) * q;
;                     }
;                 u32x4 w; w.x = cvt_pk_bf16(h[0], h[1]); w.y = cvt_pk_bf16(h[2], h[3]); w.z = cvt_pk_bf16(h[4], h[5]); w.w = cvt_pk_bf16(h[6], h[7]);
;                 *(u32x4*)(Hd + (size_t)row * ldh + u.pn * HALF + wc * 32 + 8 * fq) = w;
;             }
	v_add_f32_e32 v149, v149, v163
	v_mul_f32_e32 v163, 0xbfb8aa3b, v172
	v_mul_f32_e32 v173, v125, v163
	v_exp_f32_e32 v173, v173
	v_mul_f32_e32 v172, v124, v163
	v_exp_f32_e32 v172, v172
	v_mul_f32_e32 v125, v127, v163
	v_fma_f32 v124, v173, v171, v171
	v_mul_f32_e32 v173, v126, v163
	v_rcp_f32_e32 v124, v124
	v_exp_f32_e32 v173, v173
	v_mul_f32_e32 v126, v117, v163
	v_exp_f32_e32 v126, v126
	v_mul_f32_e32 v121, v121, v124
	v_fma_f32 v124, v173, v171, v171
	v_rcp_f32_e32 v124, v124
	v_mul_f32_e32 v117, v118, v163
	v_exp_f32_e32 v117, v117
	v_exp_f32_e32 v125, v125
	v_mul_f32_e32 v122, v122, v124
	v_mul_f32_e32 v124, v116, v163
	v_exp_f32_e32 v124, v124
	v_fma_f32 v116, v126, v171, v171
	v_rcp_f32_e32 v116, v116
	v_fma_f32 v172, v172, v171, v171
	v_fma_f32 v124, v124, v171, v171
	v_rcp_f32_e32 v124, v124
	v_mul_f32_e32 v113, v113, v116
	v_fma_f32 v116, v117, v171, v171
	v_rcp_f32_e32 v172, v172
	v_mul_f32_e32 v112, v112, v124
	v_mul_f32_e32 v124, v119, v163
	v_exp_f32_e32 v124, v124
	v_fma_f32 v125, v125, v171, v171
	v_rcp_f32_e32 v116, v116
	v_rcp_f32_e32 v125, v125
	v_fmac_f32_e32 v171, v124, v171
	v_rcp_f32_e32 v117, v171
	v_mul_f32_e32 v120, v120, v172
	v_mul_f32_e32 v118, v114, v116
	v_mul_f32_e32 v114, v119, v115
	v_mul_f32_e32 v123, v123, v125
	v_mul_f32_e32 v117, v114, v117
	v_cvt_pk_bf16_f32 v114, v120, v121
	v_cvt_pk_bf16_f32 v115, v122, v123
	v_cvt_pk_bf16_f32 v116, v112, v113
	s_add_u32 s100, s8, s22
	s_addc_u32 s101, s9, s23
	s_add_u32 s100, s100, s4
	s_addc_u32 s101, s101, s5
	v_rsq_f32_e32 v120, v161
	v_cvt_pk_bf16_f32 v117, v118, v117
	v_mad_u32_u24 v118, v162, s45, v136
	v_mul_f32_e32 v120, 0xbfb8aa3b, v120
	global_store_dwordx4 v118, v[114:117], s[100:101]
	v_mul_f32_e32 v121, v108, v120
	v_exp_f32_e32 v121, v121
	v_mul_f32_e32 v114, v109, v120
	v_exp_f32_e32 v114, v114
	v_mul_f32_e32 v109, v111, v120
	v_exp_f32_e32 v109, v109
	v_fma_f32 v115, v121, v161, v161
	v_fma_f32 v108, v114, v161, v161
	v_mul_f32_e32 v114, v110, v120
	v_rcp_f32_e32 v108, v108
	v_exp_f32_e32 v114, v114
	v_mul_f32_e32 v110, v101, v120
	v_exp_f32_e32 v110, v110
	v_mul_f32_e32 v105, v105, v108
	v_fma_f32 v108, v114, v161, v161
	v_rcp_f32_e32 v108, v108
	v_fma_f32 v109, v109, v161, v161
	v_mul_f32_e32 v101, v102, v120
	v_rcp_f32_e32 v109, v109
	v_mul_f32_e32 v106, v106, v108
	v_mul_f32_e32 v108, v100, v120
	v_exp_f32_e32 v108, v108
	v_exp_f32_e32 v101, v101
	v_mul_f32_e32 v107, v107, v109
	v_rcp_f32_e32 v115, v115
	v_fma_f32 v108, v108, v161, v161
	v_rcp_f32_e32 v108, v108
	v_rsq_f32_e32 v102, v155
	v_mul_f32_e32 v104, v104, v115
	v_fmamk_f32 v153, v153, 0x3a800000, v170
	v_mul_f32_e32 v100, v96, v108
	v_fma_f32 v96, v110, v161, v161
	v_rcp_f32_e32 v96, v96
	v_mul_f32_e32 v108, v103, v120
	v_exp_f32_e32 v108, v108
	v_mul_f32_e32 v102, 0xbfb8aa3b, v102
	v_mul_f32_e32 v109, v97, v96
	v_fma_f32 v96, v101, v161, v161
	v_rcp_f32_e32 v96, v96
	v_fmac_f32_e32 v161, v108, v161
	v_rcp_f32_e32 v97, v161
	v_mul_f32_e32 v43, v47, v43
	v_mul_f32_e32 v101, v98, v96
	v_mul_f32_e32 v96, v103, v99
	v_mul_f32_e32 v99, v96, v97
	v_cvt_pk_bf16_f32 v96, v104, v105
	v_cvt_pk_bf16_f32 v97, v106, v107
	v_cvt_pk_bf16_f32 v98, v100, v109
	v_cvt_pk_bf16_f32 v99, v101, v99
	v_mad_u32_u24 v100, v160, s45, v136
	global_store_dwordx4 v100, v[96:99], s[100:101]
	v_mul_f32_e32 v103, v92, v102
	v_exp_f32_e32 v103, v103
	v_mul_f32_e32 v96, v93, v102
	v_exp_f32_e32 v96, v96
	v_mul_f32_e32 v93, v95, v102
	v_exp_f32_e32 v93, v93
	v_fma_f32 v97, v103, v155, v155
	v_fma_f32 v92, v96, v155, v155
	v_mul_f32_e32 v96, v94, v102
	v_rcp_f32_e32 v92, v92
	v_exp_f32_e32 v96, v96
	v_mul_f32_e32 v94, v85, v102
	v_exp_f32_e32 v94, v94
	v_mul_f32_e32 v89, v89, v92
	v_fma_f32 v92, v96, v155, v155
	v_rcp_f32_e32 v92, v92
	v_fma_f32 v93, v93, v155, v155
	v_mul_f32_e32 v85, v86, v102
	v_rcp_f32_e32 v93, v93
	v_mul_f32_e32 v90, v90, v92
	v_mul_f32_e32 v92, v84, v102
	v_exp_f32_e32 v92, v92
	v_exp_f32_e32 v85, v85
	v_mul_f32_e32 v91, v91, v93
	v_rcp_f32_e32 v97, v97
	v_fma_f32 v92, v92, v155, v155
	v_rcp_f32_e32 v92, v92
	v_rsq_f32_e32 v86, v157
	v_mul_f32_e32 v88, v88, v97
	v_mul_f32_e32 v34, v38, v34
	v_mul_f32_e32 v84, v80, v92
	v_fma_f32 v80, v94, v155, v155
	v_rcp_f32_e32 v80, v80
	v_mul_f32_e32 v92, v87, v102
	v_exp_f32_e32 v92, v92
	v_mul_f32_e32 v86, 0xbfb8aa3b, v86
	v_mul_f32_e32 v93, v81, v80
	v_fma_f32 v80, v85, v155, v155
	v_rcp_f32_e32 v80, v80
	v_fmac_f32_e32 v155, v92, v155
	v_rcp_f32_e32 v81, v155
	v_fmamk_f32 v151, v151, 0x3a800000, v170
	v_mul_f32_e32 v85, v82, v80
	v_mul_f32_e32 v80, v87, v83
	v_mul_f32_e32 v83, v80, v81
	v_cvt_pk_bf16_f32 v80, v88, v89
	v_cvt_pk_bf16_f32 v81, v90, v91
	v_cvt_pk_bf16_f32 v82, v84, v93
	v_cvt_pk_bf16_f32 v83, v85, v83
	v_mad_u32_u24 v84, v158, s45, v136
	global_store_dwordx4 v84, v[80:83], s[100:101]
	v_mul_f32_e32 v87, v76, v86
	v_exp_f32_e32 v87, v87
	v_mul_f32_e32 v80, v77, v86
	v_exp_f32_e32 v80, v80
	v_mul_f32_e32 v77, v79, v86
	v_exp_f32_e32 v77, v77
	v_fma_f32 v81, v87, v157, v157
	v_fma_f32 v76, v80, v157, v157
	v_mul_f32_e32 v80, v78, v86
	v_rcp_f32_e32 v76, v76
	v_exp_f32_e32 v80, v80
	v_mul_f32_e32 v78, v69, v86
	v_exp_f32_e32 v78, v78
	v_mul_f32_e32 v73, v73, v76
	v_fma_f32 v76, v80, v157, v157
	v_rcp_f32_e32 v76, v76
	v_fma_f32 v77, v77, v157, v157
	v_mul_f32_e32 v69, v70, v86
	v_rcp_f32_e32 v77, v77
	v_mul_f32_e32 v74, v74, v76
	v_mul_f32_e32 v76, v68, v86
	v_exp_f32_e32 v76, v76
	v_exp_f32_e32 v69, v69
	v_mul_f32_e32 v75, v75, v77
	v_rcp_f32_e32 v81, v81
	v_fma_f32 v76, v76, v157, v157
	v_rcp_f32_e32 v76, v76
	v_rsq_f32_e32 v70, v159
	v_mul_f32_e32 v72, v72, v81
	v_mul_f32_e32 v24, v28, v24
	v_mul_f32_e32 v68, v64, v76
	v_fma_f32 v64, v78, v157, v157
; __device__ __forceinline__ unsigned cvt_pk_bf16(float lo, float hi) { unsigned r; asm volatile("v_cvt_pk_bf16_f32 %0, %1, %2" : "=v"(r) : "v"(lo), "v"(hi)); return r; }
;     __device__ __forceinline__ void operator()(const f32x4 (&acc)[2][2][4][2], const Unit& u, int wr, int wc, int fr, int fq) const {
;     ...
;             for (int m = 0; m < 4; ++m) {
;                 const int row = u.pm * BM + ai * HALF + wr * 64 + m * 16 + fr;
;                 const float x = xv[ai][m], rs = __builtin_amdgcn_rsqf(x);
;                 const float ea = -1.4426950408889634f * rs;
;                 float h[8];
; #pragma unroll
;                 for (int n = 0; n < 2; ++n)
; #pragma unroll
;                     for (int j = 0; j < 4; ++j) {
;                         const float g = acc[ai][0][m][n][j], uu = acc[ai][1][m][n][j];
;                         const float e = __builtin_amdgcn_exp2f(g * ea);
;                         const float q = __builtin_amdgcn_rcpf(__builtin_fmaf(e, x, x));
;                         h[n * 4 + j] = (g * uu) * q;
;                     }
;                 u32x4 w; w.x = cvt_pk_bf16(h[0], h[1]); w.y = cvt_pk_bf16(h[2], h[3]); w.z = cvt_pk_bf16(h[4], h[5]); w.w = cvt_pk_bf16(h[6], h[7]);
;                 *(u32x4*)(Hd + (size_t)row * ldh + u.pn * HALF + wc * 32 + 8 * fq) = w;
;             }
	v_rcp_f32_e32 v64, v64
	v_mul_f32_e32 v76, v71, v86
	v_exp_f32_e32 v76, v76
	v_mul_f32_e32 v70, 0xbfb8aa3b, v70
	v_mul_f32_e32 v77, v65, v64
	v_fma_f32 v64, v69, v157, v157
	v_rcp_f32_e32 v64, v64
	v_fmac_f32_e32 v157, v76, v157
	v_rcp_f32_e32 v65, v157
	v_mul_f32_e32 v25, v29, v25
	v_mul_f32_e32 v69, v66, v64
	v_mul_f32_e32 v64, v71, v67
	v_mul_f32_e32 v67, v64, v65
	v_cvt_pk_bf16_f32 v64, v72, v73
	v_cvt_pk_bf16_f32 v65, v74, v75
	v_cvt_pk_bf16_f32 v66, v68, v77
	v_cvt_pk_bf16_f32 v67, v69, v67
	v_mad_u32_u24 v68, v156, s45, v136
	global_store_dwordx4 v68, v[64:67], s[100:101]
	v_mul_f32_e32 v71, v60, v70
	v_exp_f32_e32 v71, v71
	v_mul_f32_e32 v64, v61, v70
	v_exp_f32_e32 v64, v64
	v_mul_f32_e32 v61, v63, v70
	v_exp_f32_e32 v61, v61
	v_fma_f32 v65, v71, v159, v159
	v_fma_f32 v60, v64, v159, v159
	v_mul_f32_e32 v64, v62, v70
	v_rcp_f32_e32 v60, v60
	v_exp_f32_e32 v64, v64
	v_mul_f32_e32 v62, v53, v70
	v_exp_f32_e32 v62, v62
	v_mul_f32_e32 v57, v57, v60
	v_fma_f32 v60, v64, v159, v159
	v_rcp_f32_e32 v60, v60
	v_fma_f32 v61, v61, v159, v159
	v_mul_f32_e32 v53, v54, v70
	v_rcp_f32_e32 v61, v61
	v_mul_f32_e32 v58, v58, v60
	v_mul_f32_e32 v60, v52, v70
	v_exp_f32_e32 v60, v60
	v_exp_f32_e32 v53, v53
	v_mul_f32_e32 v59, v59, v61
	v_rcp_f32_e32 v65, v65
	v_fma_f32 v60, v60, v159, v159
	v_rcp_f32_e32 v60, v60
	v_rsq_f32_e32 v54, v153
	v_mul_f32_e32 v56, v56, v65
	v_mul_f32_e32 v26, v30, v26
	v_mul_f32_e32 v52, v48, v60
	v_fma_f32 v48, v62, v159, v159
	v_rcp_f32_e32 v48, v48
	v_mul_f32_e32 v60, v55, v70
	v_exp_f32_e32 v60, v60
	v_mul_f32_e32 v54, 0xbfb8aa3b, v54
	v_mul_f32_e32 v61, v49, v48
	v_fma_f32 v48, v53, v159, v159
	v_rcp_f32_e32 v48, v48
	v_fmac_f32_e32 v159, v60, v159
	v_rcp_f32_e32 v49, v159
	v_mul_f32_e32 v16, v20, v16
	v_mul_f32_e32 v53, v50, v48
	v_mul_f32_e32 v48, v55, v51
	v_mul_f32_e32 v51, v48, v49
	v_cvt_pk_bf16_f32 v48, v56, v57
	v_cvt_pk_bf16_f32 v49, v58, v59
	v_cvt_pk_bf16_f32 v50, v52, v61
	v_cvt_pk_bf16_f32 v51, v53, v51
	v_mad_u32_u24 v52, v154, s45, v136
	global_store_dwordx4 v52, v[48:51], s[100:101]
	v_mul_f32_e32 v55, v44, v54
	v_exp_f32_e32 v55, v55
	v_mul_f32_e32 v48, v45, v54
	v_exp_f32_e32 v48, v48
	v_mul_f32_e32 v45, v47, v54
	v_exp_f32_e32 v45, v45
	v_fma_f32 v49, v55, v153, v153
	v_fma_f32 v44, v48, v153, v153
	v_mul_f32_e32 v48, v46, v54
	v_rcp_f32_e32 v44, v44
	v_exp_f32_e32 v48, v48
	v_mul_f32_e32 v46, v37, v54
	v_exp_f32_e32 v46, v46
	v_mul_f32_e32 v41, v41, v44
	v_fma_f32 v44, v48, v153, v153
	v_rcp_f32_e32 v44, v44
	v_fma_f32 v45, v45, v153, v153
	v_mul_f32_e32 v37, v38, v54
	v_rcp_f32_e32 v45, v45
	v_mul_f32_e32 v42, v42, v44
	v_mul_f32_e32 v44, v36, v54
	v_exp_f32_e32 v44, v44
	v_exp_f32_e32 v37, v37
	v_mul_f32_e32 v43, v43, v45
	v_rcp_f32_e32 v49, v49
	v_fma_f32 v44, v44, v153, v153
	v_rcp_f32_e32 v44, v44
	v_rsq_f32_e32 v38, v151
	v_mul_f32_e32 v40, v40, v49
	v_mul_f32_e32 v17, v21, v17
	v_mul_f32_e32 v36, v32, v44
	v_fma_f32 v32, v46, v153, v153
	v_rcp_f32_e32 v32, v32
	v_mul_f32_e32 v44, v39, v54
	v_exp_f32_e32 v44, v44
	v_mul_f32_e32 v38, 0xbfb8aa3b, v38
	v_mul_f32_e32 v45, v33, v32
	v_fma_f32 v32, v37, v153, v153
	v_rcp_f32_e32 v32, v32
	v_fmac_f32_e32 v153, v44, v153
	v_rcp_f32_e32 v33, v153
	v_mul_f32_e32 v27, v31, v27
	v_mul_f32_e32 v37, v34, v32
	v_mul_f32_e32 v32, v39, v35
	v_mul_f32_e32 v35, v32, v33
	v_cvt_pk_bf16_f32 v32, v40, v41
	v_cvt_pk_bf16_f32 v33, v42, v43
	v_cvt_pk_bf16_f32 v34, v36, v45
	v_cvt_pk_bf16_f32 v35, v37, v35
	v_mad_u32_u24 v36, v152, s45, v136
	global_store_dwordx4 v36, v[32:35], s[100:101]
	v_mul_f32_e32 v39, v28, v38
	v_exp_f32_e32 v39, v39
	v_mul_f32_e32 v32, v29, v38
	v_exp_f32_e32 v32, v32
	v_mul_f32_e32 v29, v31, v38
	v_exp_f32_e32 v29, v29
	v_fma_f32 v33, v39, v151, v151
	v_fma_f32 v28, v32, v151, v151
	v_mul_f32_e32 v32, v30, v38
	v_rcp_f32_e32 v28, v28
	v_exp_f32_e32 v32, v32
	v_mul_f32_e32 v30, v21, v38
	v_exp_f32_e32 v30, v30
	v_mul_f32_e32 v25, v25, v28
	v_fma_f32 v28, v32, v151, v151
	v_rcp_f32_e32 v28, v28
	v_fma_f32 v29, v29, v151, v151
	v_mul_f32_e32 v21, v22, v38
	v_rcp_f32_e32 v29, v29
	v_mul_f32_e32 v26, v26, v28
	v_mul_f32_e32 v28, v20, v38
	v_exp_f32_e32 v28, v28
	v_exp_f32_e32 v21, v21
	v_mul_f32_e32 v27, v27, v29
	v_rcp_f32_e32 v33, v33
	v_fma_f32 v28, v28, v151, v151
	v_rcp_f32_e32 v28, v28
	v_mul_f32_e32 v18, v22, v18
	v_fmamk_f32 v149, v149, 0x3a800000, v170
	v_rsq_f32_e32 v22, v149
	v_mul_f32_e32 v20, v16, v28
	v_fma_f32 v16, v30, v151, v151
	v_rcp_f32_e32 v16, v16
	v_mul_f32_e32 v28, v23, v38
	v_exp_f32_e32 v28, v28
	v_mul_f32_e32 v24, v24, v33
	v_mul_f32_e32 v29, v17, v16
	v_fma_f32 v16, v21, v151, v151
	v_rcp_f32_e32 v16, v16
	v_fmac_f32_e32 v151, v28, v151
	v_rcp_f32_e32 v17, v151
	v_mul_f32_e32 v22, 0xbfb8aa3b, v22
	v_mul_f32_e32 v21, v18, v16
	v_mul_f32_e32 v16, v23, v19
	v_mul_f32_e32 v19, v16, v17
	v_cvt_pk_bf16_f32 v16, v24, v25
	v_cvt_pk_bf16_f32 v17, v26, v27
	v_cvt_pk_bf16_f32 v18, v20, v29
	v_cvt_pk_bf16_f32 v19, v21, v19
	v_mad_u32_u24 v20, v150, s45, v136
	global_store_dwordx4 v20, v[16:19], s[100:101]
	v_mul_f32_e32 v23, v12, v22
	v_mul_f32_e32 v8, v12, v8
	v_mul_f32_e32 v16, v13, v22
	v_exp_f32_e32 v16, v16
	v_mul_f32_e32 v9, v13, v9
	v_mul_f32_e32 v10, v14, v10
	v_mul_f32_e32 v13, v15, v22
	v_fma_f32 v12, v16, v149, v149
	v_mul_f32_e32 v16, v14, v22
	v_rcp_f32_e32 v12, v12
	v_exp_f32_e32 v16, v16
	v_mul_f32_e32 v14, v5, v22
	v_exp_f32_e32 v13, v13
	v_mul_f32_e32 v9, v9, v12
	v_fma_f32 v12, v16, v149, v149
	v_rcp_f32_e32 v12, v12
	v_exp_f32_e32 v14, v14
	v_mul_f32_e32 v0, v4, v0
	v_fma_f32 v13, v13, v149, v149
	v_mul_f32_e32 v10, v10, v12
	v_mul_f32_e32 v12, v4, v22
	v_exp_f32_e32 v12, v12
	v_mul_f32_e32 v1, v5, v1
	v_mul_f32_e32 v5, v6, v22
	v_rcp_f32_e32 v13, v13
	v_fma_f32 v12, v12, v149, v149
	v_rcp_f32_e32 v12, v12
	v_exp_f32_e32 v5, v5
	v_exp_f32_e32 v23, v23
	v_mul_f32_e32 v11, v15, v11
	v_mul_f32_e32 v4, v0, v12
	v_fma_f32 v0, v14, v149, v149
	v_rcp_f32_e32 v0, v0
	v_mul_f32_e32 v12, v7, v22
	v_exp_f32_e32 v12, v12
	v_mul_f32_e32 v11, v11, v13
	v_mul_f32_e32 v13, v1, v0
	v_fma_f32 v0, v5, v149, v149
	v_fma_f32 v17, v23, v149, v149
	v_rcp_f32_e32 v0, v0
	v_fmac_f32_e32 v149, v12, v149
	v_rcp_f32_e32 v1, v149
	v_rcp_f32_e32 v17, v17
	v_mul_f32_e32 v2, v6, v2
	v_mul_f32_e32 v5, v2, v0
	v_mul_f32_e32 v0, v7, v3
	v_mul_f32_e32 v3, v0, v1
	v_mul_f32_e32 v8, v8, v17
	v_cvt_pk_bf16_f32 v0, v8, v9
	v_cvt_pk_bf16_f32 v1, v10, v11
	v_cvt_pk_bf16_f32 v2, v4, v13
	v_cvt_pk_bf16_f32 v3, v5, v3
	v_mad_u32_u24 v4, v148, s45, v136
	s_andn2_b64 vcc, exec, s[2:3]
	s_mov_b64 s[2:3], -1
	global_store_dwordx4 v4, v[0:3], s[100:101]
	s_cbranch_vccnz .LBB0_2808
	s_andn2_b64 vcc, exec, s[6:7]
	s_cbranch_vccnz .LBB0_2807
	s_barrier
	s_branch .LBB0_2807
